# v92 + residual epilogues (phase F, phase J both halves): counted vmcnt ladder per row group instead of one vmcnt(0) after the 8 x loads
# speedup vs baseline: 1.0034x; 1.0004x over previous
.LBB0_3959:
	s_lshl_b32 s0, s20, 8
	v_mov_b32_e32 v2, v247
	v_mov_b32_e32 v3, v246
	s_or_b32 s0, s0, s44
	s_lshl_b32 s20, s20, 2
	v_lshl_add_u32 v26, v2, 3, s0
	s_lshl_b32 s0, s50, 8
	s_add_i32 s0, s0, s43
	v_add_u32_e32 v28, s0, v3
	v_ashrrev_i32_e32 v27, 31, v26
	v_lshlrev_b64 v[52:53], 1, v[26:27]
	v_ashrrev_i32_e32 v29, 31, v28
	v_add_u32_e32 v40, 16, v28
	v_lshl_add_u64 v[30:31], s[8:9], 0, v[52:53]
	v_lshlrev_b64 v[54:55], 12, v[28:29]
	v_ashrrev_i32_e32 v41, 31, v40
	v_add_u32_e32 v36, 32, v28
	v_cmp_eq_u32_e32 vcc, 0, v2
	v_lshl_add_u64 v[2:3], v[30:31], 0, v[54:55]
	v_lshlrev_b64 v[42:43], 12, v[40:41]
	v_ashrrev_i32_e32 v37, 31, v36
	v_add_u32_e32 v32, 48, v28
	global_load_dwordx4 v[44:47], v[2:3], off
	global_load_dwordx4 v[48:51], v[2:3], off offset:256
	v_lshl_add_u64 v[2:3], v[30:31], 0, v[42:43]
	v_lshlrev_b64 v[38:39], 12, v[36:37]
	v_ashrrev_i32_e32 v33, 31, v32
	global_load_dwordx4 v[22:25], v[2:3], off
	global_load_dwordx4 v[18:21], v[2:3], off offset:256
	v_lshl_add_u64 v[2:3], v[30:31], 0, v[38:39]
	v_lshlrev_b64 v[34:35], 12, v[32:33]
	global_load_dwordx4 v[14:17], v[2:3], off
	global_load_dwordx4 v[10:13], v[2:3], off offset:256
	v_lshl_add_u64 v[2:3], v[30:31], 0, v[34:35]
	global_load_dwordx4 v[6:9], v[2:3], off
	s_nop 0
	global_load_dwordx4 v[2:5], v[2:3], off offset:256
	v_lshl_add_u64 v[54:55], s[8:9], 0, v[54:55]
	v_lshl_add_u64 v[52:53], v[54:55], 0, v[52:53]
	s_ashr_i32 s21, s20, 31
	s_waitcnt vmcnt(6)
	s_nop 0
	v_and_b32_e32 v57, 0xffff0000, v44
	v_lshlrev_b32_e32 v56, 16, v44
	v_and_b32_e32 v59, 0xffff0000, v45
	v_lshlrev_b32_e32 v58, 16, v45
	v_and_b32_e32 v45, 0xffff0000, v46
	v_lshlrev_b32_e32 v44, 16, v46
	v_and_b32_e32 v61, 0xffff0000, v47
	v_lshlrev_b32_e32 v60, 16, v47
	v_pk_fma_f32 v[58:59], v[192:193], s[78:79], v[58:59] op_sel_hi:[1,0,1]
	v_pk_fma_f32 v[56:57], v[190:191], s[78:79], v[56:57] op_sel_hi:[1,0,1]
	v_pk_fma_f32 v[60:61], v[188:189], s[78:79], v[60:61] op_sel_hi:[1,0,1]
	v_pk_fma_f32 v[62:63], v[186:187], s[78:79], v[44:45] op_sel_hi:[1,0,1]
	v_cvt_pk_bf16_f32 v44, v56, v57
	v_cvt_pk_bf16_f32 v45, v58, v59
	v_cvt_pk_bf16_f32 v46, v62, v63
	v_cvt_pk_bf16_f32 v47, v60, v61
	global_store_dwordx4 v[52:53], v[44:47], off
	s_nop 1
	v_mul_f32_e32 v44, v57, v57
	v_mul_f32_e32 v45, v59, v59
	v_fmac_f32_e32 v44, v56, v56
	v_fmac_f32_e32 v45, v58, v58
	v_add_f32_e32 v44, v44, v45
	v_mul_f32_e32 v45, v63, v63
	v_mul_f32_e32 v46, v61, v61
	v_fmac_f32_e32 v45, v62, v62
	v_fmac_f32_e32 v46, v60, v60
	v_add_f32_e32 v45, v45, v46
	v_add_f32_e32 v58, v44, v45
	v_and_b32_e32 v45, 0xffff0000, v48
	v_lshlrev_b32_e32 v44, 16, v48
	v_and_b32_e32 v47, 0xffff0000, v49
	v_lshlrev_b32_e32 v46, 16, v49
	v_pk_fma_f32 v[48:49], v[184:185], s[78:79], v[46:47] op_sel_hi:[1,0,1]
	v_pk_fma_f32 v[54:55], v[182:183], s[78:79], v[44:45] op_sel_hi:[1,0,1]
	v_and_b32_e32 v45, 0xffff0000, v50
	v_lshlrev_b32_e32 v44, 16, v50
	v_and_b32_e32 v47, 0xffff0000, v51
	v_lshlrev_b32_e32 v46, 16, v51
	v_pk_fma_f32 v[50:51], v[180:181], s[78:79], v[46:47] op_sel_hi:[1,0,1]
	v_pk_fma_f32 v[56:57], v[178:179], s[78:79], v[44:45] op_sel_hi:[1,0,1]
	v_cvt_pk_bf16_f32 v44, v54, v55
	v_cvt_pk_bf16_f32 v45, v48, v49
	v_cvt_pk_bf16_f32 v46, v56, v57
	v_cvt_pk_bf16_f32 v47, v50, v51
	global_store_dwordx4 v[52:53], v[44:47], off offset:256
	v_add_u32_e32 v186, 0x80, v28
	v_ashrrev_i32_e32 v187, 31, v186
	v_lshlrev_b64 v[186:187], 12, v[186:187]
	v_lshl_add_u64 v[186:187], v[30:31], 0, v[186:187]
	global_load_dwordx4 v[178:181], v[186:187], off
	global_load_dwordx4 v[182:185], v[186:187], off offset:256
	s_nop 1
	v_mul_f32_e32 v44, v55, v55
	v_mul_f32_e32 v45, v49, v49
	v_fmac_f32_e32 v44, v54, v54
	v_fmac_f32_e32 v45, v48, v48
	v_add_f32_e32 v44, v44, v45
	v_mul_f32_e32 v45, v57, v57
	v_mul_f32_e32 v46, v51, v51
	v_fmac_f32_e32 v45, v56, v56
	v_fmac_f32_e32 v46, v50, v50
	v_add_f32_e32 v45, v45, v46
	v_add_f32_e32 v44, v44, v45
	v_add_f32_e32 v44, v58, v44
	ds_bpermute_b32 v45, v249, v44
	s_waitcnt lgkmcnt(0)
	v_add_f32_e32 v44, v44, v45
	ds_bpermute_b32 v45, v250, v44
	s_and_saveexec_b64 s[22:23], vcc
	s_cbranch_execz .LBB0_3961
	v_lshlrev_b64 v[46:47], 7, v[28:29]
	v_lshl_add_u64 v[46:47], s[10:11], 0, v[46:47]
	v_lshl_add_u64 v[46:47], s[20:21], 2, v[46:47]
	s_lshl_b32 s92, s42, 2
	v_lshl_add_u64 v[46:47], v[46:47], 0, s[92:93]
	s_waitcnt lgkmcnt(0)
	v_add_f32_e32 v29, v44, v45
	global_store_dword v[46:47], v29, off
.LBB0_3961:
	s_or_b64 exec, exec, s[22:23]
	s_waitcnt lgkmcnt(0)
	s_waitcnt vmcnt(6)
	v_and_b32_e32 v45, 0xffff0000, v22
	v_lshlrev_b32_e32 v44, 16, v22
	v_and_b32_e32 v47, 0xffff0000, v23
	v_lshlrev_b32_e32 v46, 16, v23
	v_pk_fma_f32 v[44:45], v[174:175], s[78:79], v[44:45] op_sel_hi:[1,0,1]
	v_pk_fma_f32 v[46:47], v[176:177], s[78:79], v[46:47] op_sel_hi:[1,0,1]
	v_and_b32_e32 v23, 0xffff0000, v24
	v_lshlrev_b32_e32 v22, 16, v24
	v_mul_f32_e32 v29, v45, v45
	v_and_b32_e32 v49, 0xffff0000, v25
	v_lshlrev_b32_e32 v48, 16, v25
	v_pk_fma_f32 v[50:51], v[170:171], s[78:79], v[22:23] op_sel_hi:[1,0,1]
	v_cvt_pk_bf16_f32 v22, v44, v45
	v_fmac_f32_e32 v29, v44, v44
	v_mul_f32_e32 v44, v47, v47
	v_pk_fma_f32 v[48:49], v[172:173], s[78:79], v[48:49] op_sel_hi:[1,0,1]
	v_fmac_f32_e32 v44, v46, v46
	v_add_f32_e32 v29, v29, v44
	v_mul_f32_e32 v44, v51, v51
	v_mul_f32_e32 v45, v49, v49
	v_fmac_f32_e32 v44, v50, v50
	v_fmac_f32_e32 v45, v48, v48
	v_add_f32_e32 v44, v44, v45
	v_cvt_pk_bf16_f32 v23, v46, v47
	v_add_f32_e32 v29, v29, v44
	v_and_b32_e32 v45, 0xffff0000, v18
	v_and_b32_e32 v47, 0xffff0000, v19
	v_lshlrev_b32_e32 v44, 16, v18
	v_lshlrev_b32_e32 v46, 16, v19
	v_pk_fma_f32 v[46:47], v[168:169], s[78:79], v[46:47] op_sel_hi:[1,0,1]
	v_pk_fma_f32 v[18:19], v[166:167], s[78:79], v[44:45] op_sel_hi:[1,0,1]
	v_cvt_pk_bf16_f32 v25, v48, v49
	v_and_b32_e32 v45, 0xffff0000, v20
	v_and_b32_e32 v49, 0xffff0000, v21
	v_lshlrev_b32_e32 v44, 16, v20
	v_lshlrev_b32_e32 v48, 16, v21
	v_mul_f32_e32 v20, v19, v19
	v_mul_f32_e32 v21, v47, v47
	v_pk_fma_f32 v[48:49], v[164:165], s[78:79], v[48:49] op_sel_hi:[1,0,1]
	v_pk_fma_f32 v[44:45], v[162:163], s[78:79], v[44:45] op_sel_hi:[1,0,1]
	v_fmac_f32_e32 v20, v18, v18
	v_fmac_f32_e32 v21, v46, v46
	v_cvt_pk_bf16_f32 v24, v50, v51
	v_add_f32_e32 v20, v20, v21
	v_mul_f32_e32 v21, v45, v45
	v_mul_f32_e32 v50, v49, v49
	v_fmac_f32_e32 v21, v44, v44
	v_fmac_f32_e32 v50, v48, v48
	v_add_f32_e32 v21, v21, v50
	v_add_f32_e32 v20, v20, v21
	v_add_f32_e32 v29, v29, v20
	ds_bpermute_b32 v50, v249, v29
	v_lshl_add_u64 v[20:21], s[8:9], 0, v[42:43]
	v_lshl_add_u64 v[42:43], v[26:27], 1, v[20:21]
	v_cvt_pk_bf16_f32 v20, v18, v19
	global_store_dwordx4 v[42:43], v[22:25], off
	s_waitcnt lgkmcnt(0)
	v_add_f32_e32 v18, v29, v50
	ds_bpermute_b32 v19, v250, v18
	v_cvt_pk_bf16_f32 v21, v46, v47
	v_cvt_pk_bf16_f32 v22, v44, v45
	v_cvt_pk_bf16_f32 v23, v48, v49
	global_store_dwordx4 v[42:43], v[20:23], off offset:256
	v_add_u32_e32 v186, 0x90, v28
	v_ashrrev_i32_e32 v187, 31, v186
	v_lshlrev_b64 v[186:187], 12, v[186:187]
	v_lshl_add_u64 v[186:187], v[30:31], 0, v[186:187]
	global_load_dwordx4 v[162:165], v[186:187], off
	global_load_dwordx4 v[166:169], v[186:187], off offset:256
	v_add_u32_e32 v188, 0xa0, v28
	v_ashrrev_i32_e32 v189, 31, v188
	v_lshlrev_b64 v[188:189], 12, v[188:189]
	v_lshl_add_u64 v[188:189], v[30:31], 0, v[188:189]
	global_load_dwordx4 v[170:173], v[188:189], off
	global_load_dwordx4 v[174:177], v[188:189], off offset:256
	s_and_saveexec_b64 s[22:23], vcc
	s_cbranch_execz .LBB0_3963
	v_lshlrev_b64 v[20:21], 7, v[40:41]
	v_lshl_add_u64 v[20:21], s[10:11], 0, v[20:21]
	v_lshl_add_u64 v[20:21], s[20:21], 2, v[20:21]
	s_lshl_b32 s92, s42, 2
	v_lshl_add_u64 v[20:21], v[20:21], 0, s[92:93]
	s_waitcnt lgkmcnt(0)
	v_add_f32_e32 v18, v18, v19
	global_store_dword v[20:21], v18, off
.LBB0_3963:
	s_or_b64 exec, exec, s[22:23]
	s_waitcnt lgkmcnt(0)
	s_waitcnt vmcnt(8)
	v_and_b32_e32 v19, 0xffff0000, v14
	v_lshlrev_b32_e32 v18, 16, v14
	v_and_b32_e32 v21, 0xffff0000, v15
	v_lshlrev_b32_e32 v20, 16, v15
	v_pk_fma_f32 v[18:19], v[158:159], s[78:79], v[18:19] op_sel_hi:[1,0,1]
	v_and_b32_e32 v15, 0xffff0000, v16
	v_lshlrev_b32_e32 v14, 16, v16
	v_pk_fma_f32 v[20:21], v[160:161], s[78:79], v[20:21] op_sel_hi:[1,0,1]
	v_pk_fma_f32 v[24:25], v[154:155], s[78:79], v[14:15] op_sel_hi:[1,0,1]
	v_cvt_pk_bf16_f32 v14, v18, v19
	v_mul_f32_e32 v19, v19, v19
	v_and_b32_e32 v23, 0xffff0000, v17
	v_lshlrev_b32_e32 v22, 16, v17
	v_fmac_f32_e32 v19, v18, v18
	v_mul_f32_e32 v18, v21, v21
	v_pk_fma_f32 v[22:23], v[156:157], s[78:79], v[22:23] op_sel_hi:[1,0,1]
	v_fmac_f32_e32 v18, v20, v20
	v_cvt_pk_bf16_f32 v15, v20, v21
	v_add_f32_e32 v18, v19, v18
	v_mul_f32_e32 v19, v25, v25
	v_mul_f32_e32 v20, v23, v23
	v_fmac_f32_e32 v19, v24, v24
	v_fmac_f32_e32 v20, v22, v22
	v_add_f32_e32 v19, v19, v20
	v_cvt_pk_bf16_f32 v16, v24, v25
	v_add_f32_e32 v24, v18, v19
	v_and_b32_e32 v19, 0xffff0000, v10
	v_and_b32_e32 v21, 0xffff0000, v11
	v_lshlrev_b32_e32 v18, 16, v10
	v_lshlrev_b32_e32 v20, 16, v11
	v_pk_fma_f32 v[20:21], v[152:153], s[78:79], v[20:21] op_sel_hi:[1,0,1]
	v_pk_fma_f32 v[10:11], v[150:151], s[78:79], v[18:19] op_sel_hi:[1,0,1]
	v_cvt_pk_bf16_f32 v17, v22, v23
	v_and_b32_e32 v19, 0xffff0000, v12
	v_and_b32_e32 v23, 0xffff0000, v13
	v_lshlrev_b32_e32 v18, 16, v12
	v_lshlrev_b32_e32 v22, 16, v13
	v_mul_f32_e32 v12, v11, v11
	v_mul_f32_e32 v13, v21, v21
	v_pk_fma_f32 v[22:23], v[148:149], s[78:79], v[22:23] op_sel_hi:[1,0,1]
	v_pk_fma_f32 v[18:19], v[146:147], s[78:79], v[18:19] op_sel_hi:[1,0,1]
	v_fmac_f32_e32 v12, v10, v10
	v_fmac_f32_e32 v13, v20, v20
	v_add_f32_e32 v12, v12, v13
	v_mul_f32_e32 v13, v19, v19
	v_mul_f32_e32 v25, v23, v23
	v_fmac_f32_e32 v13, v18, v18
	v_fmac_f32_e32 v25, v22, v22
	v_add_f32_e32 v13, v13, v25
	v_add_f32_e32 v12, v12, v13
	v_add_f32_e32 v29, v24, v12
	ds_bpermute_b32 v40, v249, v29
	v_lshl_add_u64 v[12:13], s[8:9], 0, v[38:39]
	v_lshl_add_u64 v[24:25], v[26:27], 1, v[12:13]
	v_cvt_pk_bf16_f32 v12, v10, v11
	global_store_dwordx4 v[24:25], v[14:17], off
	s_waitcnt lgkmcnt(0)
	v_add_f32_e32 v10, v29, v40
	ds_bpermute_b32 v11, v250, v10
	v_cvt_pk_bf16_f32 v13, v20, v21
	v_cvt_pk_bf16_f32 v14, v18, v19
	v_cvt_pk_bf16_f32 v15, v22, v23
	global_store_dwordx4 v[24:25], v[12:15], off offset:256
	v_add_u32_e32 v186, 0xb0, v28
	v_ashrrev_i32_e32 v187, 31, v186
	v_lshlrev_b64 v[186:187], 12, v[186:187]
	v_lshl_add_u64 v[186:187], v[30:31], 0, v[186:187]
	global_load_dwordx4 v[146:149], v[186:187], off
	global_load_dwordx4 v[150:153], v[186:187], off offset:256
	s_and_saveexec_b64 s[22:23], vcc
	s_cbranch_execz .LBB0_3965
	v_lshlrev_b64 v[12:13], 7, v[36:37]
	v_lshl_add_u64 v[12:13], s[10:11], 0, v[12:13]
	v_lshl_add_u64 v[12:13], s[20:21], 2, v[12:13]
	s_lshl_b32 s92, s42, 2
	v_lshl_add_u64 v[12:13], v[12:13], 0, s[92:93]
	s_waitcnt lgkmcnt(0)
	v_add_f32_e32 v10, v10, v11
	global_store_dword v[12:13], v10, off
.LBB0_3965:
	s_or_b64 exec, exec, s[22:23]
	s_waitcnt lgkmcnt(0)
	s_waitcnt vmcnt(8)
	v_and_b32_e32 v11, 0xffff0000, v6
	v_lshlrev_b32_e32 v10, 16, v6
	v_and_b32_e32 v13, 0xffff0000, v7
	v_lshlrev_b32_e32 v12, 16, v7
	v_pk_fma_f32 v[10:11], v[142:143], s[78:79], v[10:11] op_sel_hi:[1,0,1]
	v_and_b32_e32 v7, 0xffff0000, v8
	v_lshlrev_b32_e32 v6, 16, v8
	v_pk_fma_f32 v[12:13], v[144:145], s[78:79], v[12:13] op_sel_hi:[1,0,1]
	v_pk_fma_f32 v[16:17], v[138:139], s[78:79], v[6:7] op_sel_hi:[1,0,1]
	v_cvt_pk_bf16_f32 v6, v10, v11
	v_mul_f32_e32 v11, v11, v11
	v_and_b32_e32 v15, 0xffff0000, v9
	v_lshlrev_b32_e32 v14, 16, v9
	v_fmac_f32_e32 v11, v10, v10
	v_mul_f32_e32 v10, v13, v13
	v_pk_fma_f32 v[14:15], v[140:141], s[78:79], v[14:15] op_sel_hi:[1,0,1]
	v_fmac_f32_e32 v10, v12, v12
	v_cvt_pk_bf16_f32 v7, v12, v13
	v_add_f32_e32 v10, v11, v10
	v_mul_f32_e32 v11, v17, v17
	v_mul_f32_e32 v12, v15, v15
	v_fmac_f32_e32 v11, v16, v16
	v_fmac_f32_e32 v12, v14, v14
	v_add_f32_e32 v11, v11, v12
	v_cvt_pk_bf16_f32 v8, v16, v17
	v_add_f32_e32 v16, v10, v11
	v_and_b32_e32 v11, 0xffff0000, v2
	v_and_b32_e32 v13, 0xffff0000, v3
	v_lshlrev_b32_e32 v10, 16, v2
	v_lshlrev_b32_e32 v12, 16, v3
	v_pk_fma_f32 v[12:13], v[136:137], s[78:79], v[12:13] op_sel_hi:[1,0,1]
	v_pk_fma_f32 v[2:3], v[134:135], s[78:79], v[10:11] op_sel_hi:[1,0,1]
	v_cvt_pk_bf16_f32 v9, v14, v15
	v_and_b32_e32 v11, 0xffff0000, v4
	v_and_b32_e32 v15, 0xffff0000, v5
	v_lshlrev_b32_e32 v10, 16, v4
	v_lshlrev_b32_e32 v14, 16, v5
	v_mul_f32_e32 v4, v3, v3
	v_mul_f32_e32 v5, v13, v13
	v_pk_fma_f32 v[14:15], v[132:133], s[78:79], v[14:15] op_sel_hi:[1,0,1]
	v_pk_fma_f32 v[10:11], v[130:131], s[78:79], v[10:11] op_sel_hi:[1,0,1]
	v_fmac_f32_e32 v4, v2, v2
	v_fmac_f32_e32 v5, v12, v12
	v_add_f32_e32 v4, v4, v5
	v_mul_f32_e32 v5, v11, v11
	v_mul_f32_e32 v17, v15, v15
	v_fmac_f32_e32 v5, v10, v10
	v_fmac_f32_e32 v17, v14, v14
	v_add_f32_e32 v5, v5, v17
	v_add_f32_e32 v4, v4, v5
	v_add_f32_e32 v18, v16, v4
	ds_bpermute_b32 v19, v249, v18
	v_lshl_add_u64 v[4:5], s[8:9], 0, v[34:35]
	v_lshl_add_u64 v[16:17], v[26:27], 1, v[4:5]
	v_cvt_pk_bf16_f32 v4, v2, v3
	global_store_dwordx4 v[16:17], v[6:9], off
	s_waitcnt lgkmcnt(0)
	v_add_f32_e32 v2, v18, v19
	ds_bpermute_b32 v3, v250, v2
	v_cvt_pk_bf16_f32 v5, v12, v13
	v_cvt_pk_bf16_f32 v6, v10, v11
	v_cvt_pk_bf16_f32 v7, v14, v15
	global_store_dwordx4 v[16:17], v[4:7], off offset:256
	s_and_saveexec_b64 s[22:23], vcc
	s_cbranch_execz .LBB0_3967
	v_lshlrev_b64 v[4:5], 7, v[32:33]
	v_lshl_add_u64 v[4:5], s[10:11], 0, v[4:5]
	v_lshl_add_u64 v[4:5], s[20:21], 2, v[4:5]
	s_lshl_b32 s92, s42, 2
	v_lshl_add_u64 v[4:5], v[4:5], 0, s[92:93]
	s_waitcnt lgkmcnt(0)
	v_add_f32_e32 v2, v2, v3
	global_store_dword v[4:5], v2, off

.LBB0_5043:
	s_lshl_b32 s0, s22, 8
	v_mov_b32_e32 v118, v246
	v_mov_b32_e32 v119, v247
	s_or_b32 s0, s0, s46
	s_lshl_b32 s22, s22, 2
	v_lshl_add_u32 v158, v119, 3, s0
	s_lshl_b32 s0, s52, 8
	s_add_i32 s0, s0, s45
	v_add_u32_e32 v160, s0, v118
	v_ashrrev_i32_e32 v159, 31, v158
	v_ashrrev_i32_e32 v161, 31, v160
	v_add_u32_e32 v172, 16, v160
	v_cmp_eq_u32_e32 vcc, 0, v119
	v_lshl_add_u64 v[162:163], v[158:159], 1, s[8:9]
	v_lshlrev_b64 v[118:119], 12, v[160:161]
	v_ashrrev_i32_e32 v173, 31, v172
	v_add_u32_e32 v168, 32, v160
	v_lshl_add_u64 v[178:179], v[162:163], 0, v[118:119]
	v_lshlrev_b64 v[118:119], 12, v[172:173]
	v_ashrrev_i32_e32 v169, 31, v168
	v_add_u32_e32 v164, 48, v160
	v_lshl_add_u64 v[174:175], v[162:163], 0, v[118:119]
	v_lshlrev_b64 v[118:119], 12, v[168:169]
	v_ashrrev_i32_e32 v165, 31, v164
	v_lshl_add_u64 v[170:171], v[162:163], 0, v[118:119]
	v_lshlrev_b64 v[118:119], 12, v[164:165]
	v_lshl_add_u64 v[166:167], v[162:163], 0, v[118:119]
	global_load_dwordx4 v[180:183], v[178:179], off
	global_load_dwordx4 v[154:157], v[178:179], off offset:256
	global_load_dwordx4 v[150:153], v[174:175], off
	global_load_dwordx4 v[138:141], v[174:175], off offset:256
	global_load_dwordx4 v[134:137], v[170:171], off
	global_load_dwordx4 v[130:133], v[170:171], off offset:256
	global_load_dwordx4 v[126:129], v[166:167], off
	global_load_dwordx4 v[118:121], v[166:167], off offset:256
	v_lshlrev_b64 v[176:177], 11, v[160:161]
	v_lshl_add_u64 v[176:177], v[176:177], 0, v[158:159]
	s_ashr_i32 s23, s22, 31
	s_waitcnt vmcnt(6)
	s_nop 0
	v_and_b32_e32 v185, 0xffff0000, v180
	v_lshlrev_b32_e32 v184, 16, v180
	v_and_b32_e32 v187, 0xffff0000, v181
	v_lshlrev_b32_e32 v186, 16, v181
	v_pk_add_f32 v[146:147], v[146:147], v[184:185]
	v_and_b32_e32 v181, 0xffff0000, v182
	v_lshlrev_b32_e32 v180, 16, v182
	v_and_b32_e32 v185, 0xffff0000, v183
	v_lshlrev_b32_e32 v184, 16, v183
	v_pk_add_f32 v[148:149], v[148:149], v[186:187]
	v_pk_add_f32 v[182:183], v[144:145], v[184:185]
	v_pk_add_f32 v[180:181], v[142:143], v[180:181]
	v_cvt_pk_bf16_f32 v142, v146, v147
	v_cvt_pk_bf16_f32 v143, v148, v149
	v_cvt_pk_bf16_f32 v144, v180, v181
	v_cvt_pk_bf16_f32 v145, v182, v183
	global_store_dwordx4 v[178:179], v[142:145], off
	s_nop 1
	v_mul_f32_e32 v142, v147, v147
	v_mul_f32_e32 v143, v149, v149
	v_fmac_f32_e32 v142, v146, v146
	v_fmac_f32_e32 v143, v148, v148
	v_add_f32_e32 v142, v142, v143
	v_mul_f32_e32 v143, v181, v181
	v_mul_f32_e32 v144, v183, v183
	v_fmac_f32_e32 v143, v180, v180
	v_fmac_f32_e32 v144, v182, v182
	v_add_f32_e32 v143, v143, v144
	v_add_f32_e32 v144, v142, v143
	v_mul_f32_e32 v142, 0x42000000, v146
	v_mul_f32_e32 v143, 0x42000000, v147
	v_med3_f32 v147, v142, s76, v237
	v_med3_f32 v143, v143, s76, v237
	v_mov_b32_e32 v142, v1
	v_cvt_pk_fp8_f32 v142, v147, v143
	v_mul_f32_e32 v145, 0x42000000, v148
	v_mul_f32_e32 v146, 0x42000000, v149
	v_med3_f32 v145, v145, s76, v237
	v_med3_f32 v146, v146, s76, v237
	v_cvt_pk_fp8_f32 v142, v145, v146 op_sel:[0,0,1]
	v_mul_f32_e32 v143, 0x42000000, v180
	v_mul_f32_e32 v145, 0x42000000, v181
	v_med3_f32 v148, v143, s76, v237
	v_med3_f32 v145, v145, s76, v237
	v_mov_b32_e32 v143, v1
	v_cvt_pk_fp8_f32 v143, v148, v145
	v_mul_f32_e32 v146, 0x42000000, v182
	v_mul_f32_e32 v147, 0x42000000, v183
	v_med3_f32 v146, v146, s76, v237
	v_med3_f32 v147, v147, s76, v237
	v_cvt_pk_fp8_f32 v143, v146, v147 op_sel:[0,0,1]
	v_and_b32_e32 v147, 0xffff0000, v154
	v_lshlrev_b32_e32 v146, 16, v154
	v_and_b32_e32 v149, 0xffff0000, v155
	v_lshlrev_b32_e32 v148, 16, v155
	v_pk_add_f32 v[124:125], v[124:125], v[148:149]
	v_pk_add_f32 v[122:123], v[122:123], v[146:147]
	v_and_b32_e32 v147, 0xffff0000, v156
	v_lshlrev_b32_e32 v146, 16, v156
	v_and_b32_e32 v149, 0xffff0000, v157
	v_lshlrev_b32_e32 v148, 16, v157
	v_pk_add_f32 v[148:149], v[116:117], v[148:149]
	v_pk_add_f32 v[146:147], v[114:115], v[146:147]
	v_cvt_pk_bf16_f32 v114, v122, v123
	v_cvt_pk_bf16_f32 v115, v124, v125
	v_cvt_pk_bf16_f32 v116, v146, v147
	v_cvt_pk_bf16_f32 v117, v148, v149
	global_store_dwordx4 v[178:179], v[114:117], off offset:256
	s_nop 1
	v_mul_f32_e32 v114, v123, v123
	v_mul_f32_e32 v115, v125, v125
	v_fmac_f32_e32 v114, v122, v122
	v_fmac_f32_e32 v115, v124, v124
	v_add_f32_e32 v114, v114, v115
	v_mul_f32_e32 v115, v147, v147
	v_mul_f32_e32 v116, v149, v149
	v_fmac_f32_e32 v115, v146, v146
	v_fmac_f32_e32 v116, v148, v148
	v_add_f32_e32 v115, v115, v116
	v_add_f32_e32 v114, v114, v115
	v_add_f32_e32 v144, v144, v114
	v_mul_f32_e32 v114, 0x42000000, v122
	v_mul_f32_e32 v115, 0x42000000, v123
	v_med3_f32 v122, v114, s76, v237
	v_med3_f32 v115, v115, s76, v237
	v_mov_b32_e32 v114, v1
	v_cvt_pk_fp8_f32 v114, v122, v115
	v_mul_f32_e32 v116, 0x42000000, v124
	v_mul_f32_e32 v117, 0x42000000, v125
	v_med3_f32 v116, v116, s76, v237
	v_med3_f32 v117, v117, s76, v237
	v_cvt_pk_fp8_f32 v114, v116, v117 op_sel:[0,0,1]
	v_mul_f32_e32 v115, 0x42000000, v146
	v_mul_f32_e32 v116, 0x42000000, v147
	v_med3_f32 v123, v115, s76, v237
	v_med3_f32 v116, v116, s76, v237
	v_mov_b32_e32 v115, v1
	v_cvt_pk_fp8_f32 v115, v123, v116
	v_mul_f32_e32 v117, 0x42000000, v148
	v_mul_f32_e32 v122, 0x42000000, v149
	v_med3_f32 v117, v117, s76, v237
	v_med3_f32 v122, v122, s76, v237
	v_cvt_pk_fp8_f32 v115, v117, v122 op_sel:[0,0,1]
	v_lshl_add_u64 v[116:117], s[10:11], 0, v[176:177]
	global_store_dwordx2 v[116:117], v[142:143], off
	global_store_dwordx2 v[116:117], v[114:115], off offset:128
	ds_bpermute_b32 v114, v249, v144
	s_waitcnt lgkmcnt(0)
	v_add_f32_e32 v114, v144, v114
	ds_bpermute_b32 v115, v250, v114
	s_and_saveexec_b64 s[24:25], vcc
	s_cbranch_execz .LBB0_5045
	v_lshlrev_b64 v[116:117], 7, v[160:161]
	v_lshl_add_u64 v[116:117], s[12:13], 0, v[116:117]
	v_lshl_add_u64 v[116:117], s[22:23], 2, v[116:117]
	s_lshl_b32 s92, s44, 2
	v_lshl_add_u64 v[116:117], v[116:117], 0, s[92:93]
	s_waitcnt lgkmcnt(0)
	v_add_f32_e32 v114, v114, v115
	global_store_dword v[116:117], v114, off
.LBB0_5045:
	s_or_b64 exec, exec, s[24:25]
	s_waitcnt vmcnt(4)
	v_and_b32_e32 v117, 0xffff0000, v150
	v_and_b32_e32 v123, 0xffff0000, v151
	v_lshlrev_b32_e32 v116, 16, v150
	v_lshlrev_b32_e32 v122, 16, v151
	v_pk_add_f32 v[112:113], v[112:113], v[122:123]
	v_pk_add_f32 v[110:111], v[110:111], v[116:117]
	v_and_b32_e32 v117, 0xffff0000, v152
	v_and_b32_e32 v123, 0xffff0000, v153
	v_lshlrev_b32_e32 v116, 16, v152
	v_lshlrev_b32_e32 v122, 16, v153
	v_pk_add_f32 v[122:123], v[108:109], v[122:123]
	v_pk_add_f32 v[116:117], v[106:107], v[116:117]
	v_cvt_pk_bf16_f32 v106, v110, v111
	v_cvt_pk_bf16_f32 v107, v112, v113
	v_cvt_pk_bf16_f32 v108, v116, v117
	v_cvt_pk_bf16_f32 v109, v122, v123
	global_store_dwordx4 v[174:175], v[106:109], off
	s_waitcnt lgkmcnt(0)
	v_lshlrev_b64 v[114:115], 11, v[172:173]
	v_lshl_add_u64 v[114:115], v[114:115], 0, v[158:159]
	v_mul_f32_e32 v106, v111, v111
	v_mul_f32_e32 v107, v113, v113
	v_fmac_f32_e32 v106, v110, v110
	v_fmac_f32_e32 v107, v112, v112
	v_add_f32_e32 v106, v106, v107
	v_mul_f32_e32 v107, v117, v117
	v_mul_f32_e32 v108, v123, v123
	v_fmac_f32_e32 v107, v116, v116
	v_fmac_f32_e32 v108, v122, v122
	v_add_f32_e32 v107, v107, v108
	v_add_f32_e32 v124, v106, v107
	v_mul_f32_e32 v106, 0x42000000, v110
	v_mul_f32_e32 v107, 0x42000000, v111
	v_med3_f32 v109, v106, s76, v237
	v_med3_f32 v107, v107, s76, v237
	v_mov_b32_e32 v106, v1
	v_cvt_pk_fp8_f32 v106, v109, v107
	v_mul_f32_e32 v108, 0x42000000, v112
	v_mul_f32_e32 v107, 0x42000000, v113
	v_med3_f32 v108, v108, s76, v237
	v_med3_f32 v107, v107, s76, v237
	v_cvt_pk_fp8_f32 v106, v108, v107 op_sel:[0,0,1]
	v_mul_f32_e32 v107, 0x42000000, v116
	v_mul_f32_e32 v108, 0x42000000, v117
	v_med3_f32 v110, v107, s76, v237
	v_med3_f32 v108, v108, s76, v237
	v_mov_b32_e32 v107, v1
	v_cvt_pk_fp8_f32 v107, v110, v108
	v_mul_f32_e32 v109, 0x42000000, v122
	v_mul_f32_e32 v108, 0x42000000, v123
	v_med3_f32 v109, v109, s76, v237
	v_med3_f32 v108, v108, s76, v237
	v_cvt_pk_fp8_f32 v107, v109, v108 op_sel:[0,0,1]
	v_and_b32_e32 v109, 0xffff0000, v138
	v_and_b32_e32 v111, 0xffff0000, v139
	v_lshlrev_b32_e32 v108, 16, v138
	v_lshlrev_b32_e32 v110, 16, v139
	v_pk_add_f32 v[104:105], v[104:105], v[110:111]
	v_pk_add_f32 v[108:109], v[102:103], v[108:109]
	v_and_b32_e32 v103, 0xffff0000, v140
	v_and_b32_e32 v111, 0xffff0000, v141
	v_lshlrev_b32_e32 v102, 16, v140
	v_lshlrev_b32_e32 v110, 16, v141
	v_mul_f32_e32 v112, v109, v109
	v_mul_f32_e32 v113, v105, v105
	v_pk_add_f32 v[110:111], v[100:101], v[110:111]
	v_pk_add_f32 v[98:99], v[98:99], v[102:103]
	v_fmac_f32_e32 v112, v108, v108
	v_fmac_f32_e32 v113, v104, v104
	v_add_f32_e32 v112, v112, v113
	v_mul_f32_e32 v113, v99, v99
	v_mul_f32_e32 v116, v111, v111
	v_fmac_f32_e32 v113, v98, v98
	v_fmac_f32_e32 v116, v110, v110
	v_cvt_pk_bf16_f32 v100, v108, v109
	v_add_f32_e32 v113, v113, v116
	v_mul_f32_e32 v108, 0x42000000, v108
	v_mul_f32_e32 v109, 0x42000000, v109
	v_cvt_pk_bf16_f32 v101, v104, v105
	v_add_f32_e32 v112, v112, v113
	v_mul_f32_e32 v113, 0x42000000, v104
	v_med3_f32 v108, v108, s76, v237
	v_med3_f32 v109, v109, s76, v237
	v_mov_b32_e32 v104, v1
	v_cvt_pk_fp8_f32 v104, v108, v109
	v_mul_f32_e32 v105, 0x42000000, v105
	v_cvt_pk_bf16_f32 v102, v98, v99
	v_med3_f32 v108, v113, s76, v237
	v_med3_f32 v105, v105, s76, v237
	v_mul_f32_e32 v98, 0x42000000, v98
	v_mul_f32_e32 v99, 0x42000000, v99
	v_add_f32_e32 v112, v124, v112
	v_cvt_pk_fp8_f32 v104, v108, v105 op_sel:[0,0,1]
	v_med3_f32 v98, v98, s76, v237
	v_med3_f32 v99, v99, s76, v237
	v_mov_b32_e32 v105, v1
	v_cvt_pk_fp8_f32 v105, v98, v99
	ds_bpermute_b32 v98, v249, v112
	v_mul_f32_e32 v108, 0x42000000, v110
	v_mul_f32_e32 v99, 0x42000000, v111
	v_med3_f32 v108, v108, s76, v237
	v_med3_f32 v99, v99, s76, v237
	s_waitcnt lgkmcnt(0)
	v_add_f32_e32 v98, v112, v98
	v_cvt_pk_fp8_f32 v105, v108, v99 op_sel:[0,0,1]
	ds_bpermute_b32 v99, v250, v98
	v_cvt_pk_bf16_f32 v103, v110, v111
	global_store_dwordx4 v[174:175], v[100:103], off offset:256
	s_nop 1
	v_lshl_add_u64 v[100:101], s[10:11], 0, v[114:115]
	global_store_dwordx2 v[100:101], v[106:107], off
	global_store_dwordx2 v[100:101], v[104:105], off offset:128
	s_and_saveexec_b64 s[24:25], vcc
	s_cbranch_execz .LBB0_5047
	v_lshlrev_b64 v[100:101], 7, v[172:173]
	v_lshl_add_u64 v[100:101], s[12:13], 0, v[100:101]
	v_lshl_add_u64 v[100:101], s[22:23], 2, v[100:101]
	s_lshl_b32 s92, s44, 2
	v_lshl_add_u64 v[100:101], v[100:101], 0, s[92:93]
	s_waitcnt lgkmcnt(0)
	v_add_f32_e32 v98, v98, v99
	global_store_dword v[100:101], v98, off
.LBB0_5047:
	s_or_b64 exec, exec, s[24:25]
	s_waitcnt vmcnt(2)
	v_and_b32_e32 v101, 0xffff0000, v134
	v_and_b32_e32 v103, 0xffff0000, v135
	v_lshlrev_b32_e32 v100, 16, v134
	v_lshlrev_b32_e32 v102, 16, v135
	v_pk_add_f32 v[96:97], v[96:97], v[102:103]
	v_pk_add_f32 v[94:95], v[94:95], v[100:101]
	v_and_b32_e32 v101, 0xffff0000, v136
	v_and_b32_e32 v103, 0xffff0000, v137
	v_lshlrev_b32_e32 v100, 16, v136
	v_lshlrev_b32_e32 v102, 16, v137
	v_pk_add_f32 v[102:103], v[92:93], v[102:103]
	v_pk_add_f32 v[100:101], v[90:91], v[100:101]
	v_cvt_pk_bf16_f32 v90, v94, v95
	v_cvt_pk_bf16_f32 v91, v96, v97
	v_cvt_pk_bf16_f32 v92, v100, v101
	v_cvt_pk_bf16_f32 v93, v102, v103
	global_store_dwordx4 v[170:171], v[90:93], off
	s_waitcnt lgkmcnt(0)
	v_lshlrev_b64 v[98:99], 11, v[168:169]
	v_lshl_add_u64 v[98:99], v[98:99], 0, v[158:159]
	v_mul_f32_e32 v90, v95, v95
	v_mul_f32_e32 v91, v97, v97
	v_fmac_f32_e32 v90, v94, v94
	v_fmac_f32_e32 v91, v96, v96
	v_add_f32_e32 v90, v90, v91
	v_mul_f32_e32 v91, v101, v101
	v_mul_f32_e32 v92, v103, v103
	v_fmac_f32_e32 v91, v100, v100
	v_fmac_f32_e32 v92, v102, v102
	v_add_f32_e32 v91, v91, v92
	v_add_f32_e32 v104, v90, v91
	v_mul_f32_e32 v90, 0x42000000, v94
	v_mul_f32_e32 v91, 0x42000000, v95
	v_med3_f32 v93, v90, s76, v237
	v_med3_f32 v91, v91, s76, v237
	v_mov_b32_e32 v90, v1
	v_cvt_pk_fp8_f32 v90, v93, v91
	v_mul_f32_e32 v92, 0x42000000, v96
	v_mul_f32_e32 v91, 0x42000000, v97
	v_med3_f32 v92, v92, s76, v237
	v_med3_f32 v91, v91, s76, v237
	v_cvt_pk_fp8_f32 v90, v92, v91 op_sel:[0,0,1]
	v_mul_f32_e32 v91, 0x42000000, v100
	v_mul_f32_e32 v92, 0x42000000, v101
	v_med3_f32 v94, v91, s76, v237
	v_med3_f32 v92, v92, s76, v237
	v_mov_b32_e32 v91, v1
	v_cvt_pk_fp8_f32 v91, v94, v92
	v_mul_f32_e32 v93, 0x42000000, v102
	v_mul_f32_e32 v92, 0x42000000, v103
	v_med3_f32 v93, v93, s76, v237
	v_med3_f32 v92, v92, s76, v237
	v_cvt_pk_fp8_f32 v91, v93, v92 op_sel:[0,0,1]
	v_and_b32_e32 v93, 0xffff0000, v130
	v_and_b32_e32 v95, 0xffff0000, v131
	v_lshlrev_b32_e32 v92, 16, v130
	v_lshlrev_b32_e32 v94, 16, v131
	v_pk_add_f32 v[88:89], v[88:89], v[94:95]
	v_pk_add_f32 v[92:93], v[86:87], v[92:93]
	v_and_b32_e32 v87, 0xffff0000, v132
	v_and_b32_e32 v95, 0xffff0000, v133
	v_lshlrev_b32_e32 v86, 16, v132
	v_lshlrev_b32_e32 v94, 16, v133
	v_mul_f32_e32 v96, v93, v93
	v_mul_f32_e32 v97, v89, v89
	v_pk_add_f32 v[94:95], v[84:85], v[94:95]
	v_pk_add_f32 v[82:83], v[82:83], v[86:87]
	v_fmac_f32_e32 v96, v92, v92
	v_fmac_f32_e32 v97, v88, v88
	v_add_f32_e32 v96, v96, v97
	v_mul_f32_e32 v97, v83, v83
	v_mul_f32_e32 v100, v95, v95
	v_fmac_f32_e32 v97, v82, v82
	v_fmac_f32_e32 v100, v94, v94
	v_cvt_pk_bf16_f32 v84, v92, v93
	v_add_f32_e32 v97, v97, v100
	v_mul_f32_e32 v92, 0x42000000, v92
	v_mul_f32_e32 v93, 0x42000000, v93
	v_cvt_pk_bf16_f32 v85, v88, v89
	v_add_f32_e32 v96, v96, v97
	v_mul_f32_e32 v97, 0x42000000, v88
	v_med3_f32 v92, v92, s76, v237
	v_med3_f32 v93, v93, s76, v237
	v_mov_b32_e32 v88, v1
	v_cvt_pk_fp8_f32 v88, v92, v93
	v_mul_f32_e32 v89, 0x42000000, v89
	v_cvt_pk_bf16_f32 v86, v82, v83
	v_med3_f32 v92, v97, s76, v237
	v_med3_f32 v89, v89, s76, v237
	v_mul_f32_e32 v82, 0x42000000, v82
	v_mul_f32_e32 v83, 0x42000000, v83
	v_add_f32_e32 v96, v104, v96
	v_cvt_pk_fp8_f32 v88, v92, v89 op_sel:[0,0,1]
	v_med3_f32 v82, v82, s76, v237
	v_med3_f32 v83, v83, s76, v237
	v_mov_b32_e32 v89, v1
	v_cvt_pk_fp8_f32 v89, v82, v83
	ds_bpermute_b32 v82, v249, v96
	v_mul_f32_e32 v92, 0x42000000, v94
	v_mul_f32_e32 v83, 0x42000000, v95
	v_med3_f32 v92, v92, s76, v237
	v_med3_f32 v83, v83, s76, v237
	s_waitcnt lgkmcnt(0)
	v_add_f32_e32 v82, v96, v82
	v_cvt_pk_fp8_f32 v89, v92, v83 op_sel:[0,0,1]
	ds_bpermute_b32 v83, v250, v82
	v_cvt_pk_bf16_f32 v87, v94, v95
	global_store_dwordx4 v[170:171], v[84:87], off offset:256
	s_nop 1
	v_lshl_add_u64 v[84:85], s[10:11], 0, v[98:99]
	global_store_dwordx2 v[84:85], v[90:91], off
	global_store_dwordx2 v[84:85], v[88:89], off offset:128
	s_and_saveexec_b64 s[24:25], vcc
	s_cbranch_execz .LBB0_5049
	v_lshlrev_b64 v[84:85], 7, v[168:169]
	v_lshl_add_u64 v[84:85], s[12:13], 0, v[84:85]
	v_lshl_add_u64 v[84:85], s[22:23], 2, v[84:85]
	s_lshl_b32 s92, s44, 2
	v_lshl_add_u64 v[84:85], v[84:85], 0, s[92:93]
	s_waitcnt lgkmcnt(0)
	v_add_f32_e32 v82, v82, v83
	global_store_dword v[84:85], v82, off
.LBB0_5049:
	s_or_b64 exec, exec, s[24:25]
	s_waitcnt vmcnt(0)
	v_and_b32_e32 v85, 0xffff0000, v126
	v_and_b32_e32 v87, 0xffff0000, v127
	v_lshlrev_b32_e32 v84, 16, v126
	v_lshlrev_b32_e32 v86, 16, v127
	v_pk_add_f32 v[80:81], v[80:81], v[86:87]
	v_pk_add_f32 v[78:79], v[78:79], v[84:85]
	v_and_b32_e32 v85, 0xffff0000, v128
	v_and_b32_e32 v87, 0xffff0000, v129
	v_lshlrev_b32_e32 v84, 16, v128
	v_lshlrev_b32_e32 v86, 16, v129
	v_pk_add_f32 v[86:87], v[76:77], v[86:87]
	v_pk_add_f32 v[84:85], v[74:75], v[84:85]
	v_cvt_pk_bf16_f32 v74, v78, v79
	v_cvt_pk_bf16_f32 v75, v80, v81
	v_cvt_pk_bf16_f32 v76, v84, v85
	v_cvt_pk_bf16_f32 v77, v86, v87
	global_store_dwordx4 v[166:167], v[74:77], off
	s_waitcnt lgkmcnt(0)
	v_lshlrev_b64 v[82:83], 11, v[164:165]
	v_lshl_add_u64 v[82:83], v[82:83], 0, v[158:159]
	v_mul_f32_e32 v74, v79, v79
	v_mul_f32_e32 v75, v81, v81
	v_fmac_f32_e32 v74, v78, v78
	v_fmac_f32_e32 v75, v80, v80
	v_add_f32_e32 v74, v74, v75
	v_mul_f32_e32 v75, v85, v85
	v_mul_f32_e32 v76, v87, v87
	v_fmac_f32_e32 v75, v84, v84
	v_fmac_f32_e32 v76, v86, v86
	v_add_f32_e32 v75, v75, v76
	v_add_f32_e32 v88, v74, v75
	v_mul_f32_e32 v74, 0x42000000, v78
	v_mul_f32_e32 v75, 0x42000000, v79
	v_med3_f32 v77, v74, s76, v237
	v_med3_f32 v75, v75, s76, v237
	v_mov_b32_e32 v74, v1
	v_cvt_pk_fp8_f32 v74, v77, v75
	v_mul_f32_e32 v76, 0x42000000, v80
	v_mul_f32_e32 v75, 0x42000000, v81
	v_med3_f32 v76, v76, s76, v237
	v_med3_f32 v75, v75, s76, v237
	v_cvt_pk_fp8_f32 v74, v76, v75 op_sel:[0,0,1]
	v_mul_f32_e32 v75, 0x42000000, v84
	v_mul_f32_e32 v76, 0x42000000, v85
	v_med3_f32 v78, v75, s76, v237
	v_med3_f32 v76, v76, s76, v237
	v_mov_b32_e32 v75, v1
	v_cvt_pk_fp8_f32 v75, v78, v76
	v_mul_f32_e32 v77, 0x42000000, v86
	v_mul_f32_e32 v76, 0x42000000, v87
	v_med3_f32 v77, v77, s76, v237
	v_med3_f32 v76, v76, s76, v237
	v_cvt_pk_fp8_f32 v75, v77, v76 op_sel:[0,0,1]
	v_and_b32_e32 v77, 0xffff0000, v118
	v_and_b32_e32 v79, 0xffff0000, v119
	v_lshlrev_b32_e32 v76, 16, v118
	v_lshlrev_b32_e32 v78, 16, v119
	v_pk_add_f32 v[72:73], v[72:73], v[78:79]
	v_pk_add_f32 v[76:77], v[70:71], v[76:77]
	v_and_b32_e32 v71, 0xffff0000, v120
	v_and_b32_e32 v79, 0xffff0000, v121
	v_lshlrev_b32_e32 v70, 16, v120
	v_lshlrev_b32_e32 v78, 16, v121
	v_mul_f32_e32 v80, v77, v77
	v_mul_f32_e32 v81, v73, v73
	v_pk_add_f32 v[78:79], v[68:69], v[78:79]
	v_pk_add_f32 v[66:67], v[66:67], v[70:71]
	v_fmac_f32_e32 v80, v76, v76
	v_fmac_f32_e32 v81, v72, v72
	v_add_f32_e32 v80, v80, v81
	v_mul_f32_e32 v81, v67, v67
	v_mul_f32_e32 v84, v79, v79
	v_fmac_f32_e32 v81, v66, v66
	v_fmac_f32_e32 v84, v78, v78
	v_cvt_pk_bf16_f32 v68, v76, v77
	v_add_f32_e32 v81, v81, v84
	v_mul_f32_e32 v76, 0x42000000, v76
	v_mul_f32_e32 v77, 0x42000000, v77
	v_cvt_pk_bf16_f32 v69, v72, v73
	v_add_f32_e32 v80, v80, v81
	v_mul_f32_e32 v81, 0x42000000, v72
	v_med3_f32 v76, v76, s76, v237
	v_med3_f32 v77, v77, s76, v237
	v_mov_b32_e32 v72, v1
	v_cvt_pk_fp8_f32 v72, v76, v77
	v_mul_f32_e32 v73, 0x42000000, v73
	v_cvt_pk_bf16_f32 v70, v66, v67
	v_med3_f32 v76, v81, s76, v237
	v_med3_f32 v73, v73, s76, v237
	v_mul_f32_e32 v66, 0x42000000, v66
	v_mul_f32_e32 v67, 0x42000000, v67
	v_add_f32_e32 v80, v88, v80
	v_cvt_pk_fp8_f32 v72, v76, v73 op_sel:[0,0,1]
	v_med3_f32 v66, v66, s76, v237
	v_med3_f32 v67, v67, s76, v237
	v_mov_b32_e32 v73, v1
	v_cvt_pk_fp8_f32 v73, v66, v67
	ds_bpermute_b32 v66, v249, v80
	v_mul_f32_e32 v76, 0x42000000, v78
	v_mul_f32_e32 v67, 0x42000000, v79
	v_med3_f32 v76, v76, s76, v237
	v_med3_f32 v67, v67, s76, v237
	s_waitcnt lgkmcnt(0)
	v_add_f32_e32 v66, v80, v66
	v_cvt_pk_fp8_f32 v73, v76, v67 op_sel:[0,0,1]
	ds_bpermute_b32 v67, v250, v66
	v_cvt_pk_bf16_f32 v71, v78, v79
	global_store_dwordx4 v[166:167], v[68:71], off offset:256
	s_nop 1
	v_lshl_add_u64 v[68:69], s[10:11], 0, v[82:83]
	global_store_dwordx2 v[68:69], v[74:75], off
	global_store_dwordx2 v[68:69], v[72:73], off offset:128
	s_and_saveexec_b64 s[24:25], vcc
	s_cbranch_execz .LBB0_5051
	v_lshlrev_b64 v[68:69], 7, v[164:165]
	v_lshl_add_u64 v[68:69], s[12:13], 0, v[68:69]
	v_lshl_add_u64 v[68:69], s[22:23], 2, v[68:69]
	s_lshl_b32 s92, s44, 2
	v_lshl_add_u64 v[68:69], v[68:69], 0, s[92:93]
	s_waitcnt lgkmcnt(0)
	v_add_f32_e32 v66, v66, v67
	global_store_dword v[68:69], v66, off
.LBB0_5051:
	s_or_b64 exec, exec, s[24:25]
	v_add_u32_e32 v106, 0x80, v160
	v_ashrrev_i32_e32 v107, 31, v106
	v_add_u32_e32 v102, 0x90, v160
	s_waitcnt lgkmcnt(0)
	v_lshlrev_b64 v[66:67], 12, v[106:107]
	v_ashrrev_i32_e32 v103, 31, v102
	v_add_u32_e32 v98, 0xa0, v160
	v_lshl_add_u64 v[110:111], v[162:163], 0, v[66:67]
	v_lshlrev_b64 v[66:67], 12, v[102:103]
	v_ashrrev_i32_e32 v99, 31, v98
	v_add_u32_e32 v94, 0xb0, v160
	v_lshl_add_u64 v[104:105], v[162:163], 0, v[66:67]
	v_lshlrev_b64 v[66:67], 12, v[98:99]
	v_ashrrev_i32_e32 v95, 31, v94
	v_lshl_add_u64 v[100:101], v[162:163], 0, v[66:67]
	v_lshlrev_b64 v[66:67], 12, v[94:95]
	v_lshl_add_u64 v[96:97], v[162:163], 0, v[66:67]
	global_load_dwordx4 v[112:115], v[110:111], off
	global_load_dwordx4 v[90:93], v[110:111], off offset:256
	global_load_dwordx4 v[86:89], v[104:105], off
	global_load_dwordx4 v[82:85], v[104:105], off offset:256
	global_load_dwordx4 v[78:81], v[100:101], off
	global_load_dwordx4 v[74:77], v[100:101], off offset:256
	global_load_dwordx4 v[70:73], v[96:97], off
	global_load_dwordx4 v[66:69], v[96:97], off offset:256
	v_lshlrev_b64 v[108:109], 11, v[106:107]
	v_lshl_add_u64 v[108:109], v[108:109], 0, v[158:159]
	s_waitcnt vmcnt(6)
	s_nop 0
	v_and_b32_e32 v117, 0xffff0000, v112
	v_lshlrev_b32_e32 v116, 16, v112
	v_and_b32_e32 v119, 0xffff0000, v113
	v_lshlrev_b32_e32 v118, 16, v113
	v_pk_add_f32 v[62:63], v[62:63], v[116:117]
	v_and_b32_e32 v113, 0xffff0000, v114
	v_lshlrev_b32_e32 v112, 16, v114
	v_and_b32_e32 v117, 0xffff0000, v115
	v_lshlrev_b32_e32 v116, 16, v115
	v_pk_add_f32 v[64:65], v[64:65], v[118:119]
	v_pk_add_f32 v[114:115], v[60:61], v[116:117]
	v_pk_add_f32 v[112:113], v[58:59], v[112:113]
	v_cvt_pk_bf16_f32 v58, v62, v63
	v_cvt_pk_bf16_f32 v59, v64, v65
	v_cvt_pk_bf16_f32 v60, v112, v113
	v_cvt_pk_bf16_f32 v61, v114, v115
	global_store_dwordx4 v[110:111], v[58:61], off
	s_nop 1
	v_mul_f32_e32 v58, v63, v63
	v_mul_f32_e32 v59, v65, v65
	v_fmac_f32_e32 v58, v62, v62
	v_fmac_f32_e32 v59, v64, v64
	v_add_f32_e32 v58, v58, v59
	v_mul_f32_e32 v59, v113, v113
	v_mul_f32_e32 v60, v115, v115
	v_fmac_f32_e32 v59, v112, v112
	v_fmac_f32_e32 v60, v114, v114
	v_add_f32_e32 v59, v59, v60
	v_add_f32_e32 v60, v58, v59
	v_mul_f32_e32 v58, 0x42000000, v62
	v_mul_f32_e32 v59, 0x42000000, v63
	v_med3_f32 v63, v58, s76, v237
	v_med3_f32 v59, v59, s76, v237
	v_mov_b32_e32 v58, v1
	v_cvt_pk_fp8_f32 v58, v63, v59
	v_mul_f32_e32 v61, 0x42000000, v64
	v_mul_f32_e32 v62, 0x42000000, v65
	v_med3_f32 v61, v61, s76, v237
	v_med3_f32 v62, v62, s76, v237
	v_cvt_pk_fp8_f32 v58, v61, v62 op_sel:[0,0,1]
	v_mul_f32_e32 v59, 0x42000000, v112
	v_mul_f32_e32 v61, 0x42000000, v113
	v_med3_f32 v64, v59, s76, v237
	v_med3_f32 v61, v61, s76, v237
	v_mov_b32_e32 v59, v1
	v_cvt_pk_fp8_f32 v59, v64, v61
	v_mul_f32_e32 v62, 0x42000000, v114
	v_mul_f32_e32 v63, 0x42000000, v115
	v_med3_f32 v62, v62, s76, v237
	v_med3_f32 v63, v63, s76, v237
	v_cvt_pk_fp8_f32 v59, v62, v63 op_sel:[0,0,1]
	v_and_b32_e32 v63, 0xffff0000, v90
	v_lshlrev_b32_e32 v62, 16, v90
	v_and_b32_e32 v65, 0xffff0000, v91
	v_lshlrev_b32_e32 v64, 16, v91
	v_pk_add_f32 v[56:57], v[56:57], v[64:65]
	v_pk_add_f32 v[54:55], v[54:55], v[62:63]
	v_and_b32_e32 v63, 0xffff0000, v92
	v_lshlrev_b32_e32 v62, 16, v92
	v_and_b32_e32 v65, 0xffff0000, v93
	v_lshlrev_b32_e32 v64, 16, v93
	v_pk_add_f32 v[64:65], v[52:53], v[64:65]
	v_pk_add_f32 v[62:63], v[50:51], v[62:63]
	v_cvt_pk_bf16_f32 v50, v54, v55
	v_cvt_pk_bf16_f32 v51, v56, v57
	v_cvt_pk_bf16_f32 v52, v62, v63
	v_cvt_pk_bf16_f32 v53, v64, v65
	global_store_dwordx4 v[110:111], v[50:53], off offset:256
	s_nop 1
	v_mul_f32_e32 v50, v55, v55
	v_mul_f32_e32 v51, v57, v57
	v_fmac_f32_e32 v50, v54, v54
	v_fmac_f32_e32 v51, v56, v56
	v_add_f32_e32 v50, v50, v51
	v_mul_f32_e32 v51, v63, v63
	v_mul_f32_e32 v52, v65, v65
	v_fmac_f32_e32 v51, v62, v62
	v_fmac_f32_e32 v52, v64, v64
	v_add_f32_e32 v51, v51, v52
	v_add_f32_e32 v50, v50, v51
	v_add_f32_e32 v60, v60, v50
	v_mul_f32_e32 v50, 0x42000000, v54
	v_mul_f32_e32 v51, 0x42000000, v55
	v_med3_f32 v54, v50, s76, v237
	v_med3_f32 v51, v51, s76, v237
	v_mov_b32_e32 v50, v1
	v_cvt_pk_fp8_f32 v50, v54, v51
	v_mul_f32_e32 v52, 0x42000000, v56
	v_mul_f32_e32 v53, 0x42000000, v57
	v_med3_f32 v52, v52, s76, v237
	v_med3_f32 v53, v53, s76, v237
	v_cvt_pk_fp8_f32 v50, v52, v53 op_sel:[0,0,1]
	v_mul_f32_e32 v51, 0x42000000, v62
	v_mul_f32_e32 v52, 0x42000000, v63
	v_med3_f32 v55, v51, s76, v237
	v_med3_f32 v52, v52, s76, v237
	v_mov_b32_e32 v51, v1
	v_cvt_pk_fp8_f32 v51, v55, v52
	v_mul_f32_e32 v53, 0x42000000, v64
	v_mul_f32_e32 v54, 0x42000000, v65
	v_med3_f32 v53, v53, s76, v237
	v_med3_f32 v54, v54, s76, v237
	v_cvt_pk_fp8_f32 v51, v53, v54 op_sel:[0,0,1]
	v_lshl_add_u64 v[52:53], s[10:11], 0, v[108:109]
	global_store_dwordx2 v[52:53], v[58:59], off
	global_store_dwordx2 v[52:53], v[50:51], off offset:128
	ds_bpermute_b32 v50, v249, v60
	s_waitcnt lgkmcnt(0)
	v_add_f32_e32 v50, v60, v50
	ds_bpermute_b32 v51, v250, v50
	s_and_saveexec_b64 s[24:25], vcc
	s_cbranch_execz .LBB0_5053
	v_lshlrev_b64 v[52:53], 7, v[106:107]
	v_lshl_add_u64 v[52:53], s[12:13], 0, v[52:53]
	v_lshl_add_u64 v[52:53], s[22:23], 2, v[52:53]
	s_lshl_b32 s92, s44, 2
	v_lshl_add_u64 v[52:53], v[52:53], 0, s[92:93]
	s_waitcnt lgkmcnt(0)
	v_add_f32_e32 v50, v50, v51
	global_store_dword v[52:53], v50, off
.LBB0_5053:
	s_or_b64 exec, exec, s[24:25]
	s_waitcnt vmcnt(4)
	v_and_b32_e32 v53, 0xffff0000, v86
	v_and_b32_e32 v55, 0xffff0000, v87
	v_lshlrev_b32_e32 v52, 16, v86
	v_lshlrev_b32_e32 v54, 16, v87
	v_pk_add_f32 v[48:49], v[48:49], v[54:55]
	v_pk_add_f32 v[46:47], v[46:47], v[52:53]
	v_and_b32_e32 v53, 0xffff0000, v88
	v_and_b32_e32 v55, 0xffff0000, v89
	v_lshlrev_b32_e32 v52, 16, v88
	v_lshlrev_b32_e32 v54, 16, v89
	v_pk_add_f32 v[54:55], v[44:45], v[54:55]
	v_pk_add_f32 v[52:53], v[42:43], v[52:53]
	v_cvt_pk_bf16_f32 v42, v46, v47
	v_cvt_pk_bf16_f32 v43, v48, v49
	v_cvt_pk_bf16_f32 v44, v52, v53
	v_cvt_pk_bf16_f32 v45, v54, v55
	global_store_dwordx4 v[104:105], v[42:45], off
	s_waitcnt lgkmcnt(0)
	v_lshlrev_b64 v[50:51], 11, v[102:103]
	v_lshl_add_u64 v[50:51], v[50:51], 0, v[158:159]
	v_mul_f32_e32 v42, v47, v47
	v_mul_f32_e32 v43, v49, v49
	v_fmac_f32_e32 v42, v46, v46
	v_fmac_f32_e32 v43, v48, v48
	v_add_f32_e32 v42, v42, v43
	v_mul_f32_e32 v43, v53, v53
	v_mul_f32_e32 v44, v55, v55
	v_fmac_f32_e32 v43, v52, v52
	v_fmac_f32_e32 v44, v54, v54
	v_add_f32_e32 v43, v43, v44
	v_add_f32_e32 v56, v42, v43
	v_mul_f32_e32 v42, 0x42000000, v46
	v_mul_f32_e32 v43, 0x42000000, v47
	v_med3_f32 v45, v42, s76, v237
	v_med3_f32 v43, v43, s76, v237
	v_mov_b32_e32 v42, v1
	v_cvt_pk_fp8_f32 v42, v45, v43
	v_mul_f32_e32 v44, 0x42000000, v48
	v_mul_f32_e32 v43, 0x42000000, v49
	v_med3_f32 v44, v44, s76, v237
	v_med3_f32 v43, v43, s76, v237
	v_cvt_pk_fp8_f32 v42, v44, v43 op_sel:[0,0,1]
	v_mul_f32_e32 v43, 0x42000000, v52
	v_mul_f32_e32 v44, 0x42000000, v53
	v_med3_f32 v46, v43, s76, v237
	v_med3_f32 v44, v44, s76, v237
	v_mov_b32_e32 v43, v1
	v_cvt_pk_fp8_f32 v43, v46, v44
	v_mul_f32_e32 v45, 0x42000000, v54
	v_mul_f32_e32 v44, 0x42000000, v55
	v_med3_f32 v45, v45, s76, v237
	v_med3_f32 v44, v44, s76, v237
	v_cvt_pk_fp8_f32 v43, v45, v44 op_sel:[0,0,1]
	v_and_b32_e32 v45, 0xffff0000, v82
	v_and_b32_e32 v47, 0xffff0000, v83
	v_lshlrev_b32_e32 v44, 16, v82
	v_lshlrev_b32_e32 v46, 16, v83
	v_pk_add_f32 v[40:41], v[40:41], v[46:47]
	v_pk_add_f32 v[44:45], v[38:39], v[44:45]
	v_and_b32_e32 v39, 0xffff0000, v84
	v_and_b32_e32 v47, 0xffff0000, v85
	v_lshlrev_b32_e32 v38, 16, v84
	v_lshlrev_b32_e32 v46, 16, v85
	v_mul_f32_e32 v48, v45, v45
	v_mul_f32_e32 v49, v41, v41
	v_pk_add_f32 v[46:47], v[36:37], v[46:47]
	v_pk_add_f32 v[34:35], v[34:35], v[38:39]
	v_fmac_f32_e32 v48, v44, v44
	v_fmac_f32_e32 v49, v40, v40
	v_add_f32_e32 v48, v48, v49
	v_mul_f32_e32 v49, v35, v35
	v_mul_f32_e32 v52, v47, v47
	v_fmac_f32_e32 v49, v34, v34
	v_fmac_f32_e32 v52, v46, v46
	v_cvt_pk_bf16_f32 v36, v44, v45
	v_add_f32_e32 v49, v49, v52
	v_mul_f32_e32 v44, 0x42000000, v44
	v_mul_f32_e32 v45, 0x42000000, v45
	v_cvt_pk_bf16_f32 v37, v40, v41
	v_add_f32_e32 v48, v48, v49
	v_mul_f32_e32 v49, 0x42000000, v40
	v_med3_f32 v44, v44, s76, v237
	v_med3_f32 v45, v45, s76, v237
	v_mov_b32_e32 v40, v1
	v_cvt_pk_fp8_f32 v40, v44, v45
	v_mul_f32_e32 v41, 0x42000000, v41
	v_cvt_pk_bf16_f32 v38, v34, v35
	v_med3_f32 v44, v49, s76, v237
	v_med3_f32 v41, v41, s76, v237
	v_mul_f32_e32 v34, 0x42000000, v34
	v_mul_f32_e32 v35, 0x42000000, v35
	v_add_f32_e32 v48, v56, v48
	v_cvt_pk_fp8_f32 v40, v44, v41 op_sel:[0,0,1]
	v_med3_f32 v34, v34, s76, v237
	v_med3_f32 v35, v35, s76, v237
	v_mov_b32_e32 v41, v1
	v_cvt_pk_fp8_f32 v41, v34, v35
	ds_bpermute_b32 v34, v249, v48
	v_mul_f32_e32 v44, 0x42000000, v46
	v_mul_f32_e32 v35, 0x42000000, v47
	v_med3_f32 v44, v44, s76, v237
	v_med3_f32 v35, v35, s76, v237
	s_waitcnt lgkmcnt(0)
	v_add_f32_e32 v34, v48, v34
	v_cvt_pk_fp8_f32 v41, v44, v35 op_sel:[0,0,1]
	ds_bpermute_b32 v35, v250, v34
	v_cvt_pk_bf16_f32 v39, v46, v47
	global_store_dwordx4 v[104:105], v[36:39], off offset:256
	s_nop 1
	v_lshl_add_u64 v[36:37], s[10:11], 0, v[50:51]
	global_store_dwordx2 v[36:37], v[42:43], off
	global_store_dwordx2 v[36:37], v[40:41], off offset:128
	s_and_saveexec_b64 s[24:25], vcc
	s_cbranch_execz .LBB0_5055
	v_lshlrev_b64 v[36:37], 7, v[102:103]
	v_lshl_add_u64 v[36:37], s[12:13], 0, v[36:37]
	v_lshl_add_u64 v[36:37], s[22:23], 2, v[36:37]
	s_lshl_b32 s92, s44, 2
	v_lshl_add_u64 v[36:37], v[36:37], 0, s[92:93]
	s_waitcnt lgkmcnt(0)
	v_add_f32_e32 v34, v34, v35
	global_store_dword v[36:37], v34, off
.LBB0_5055:
	s_or_b64 exec, exec, s[24:25]
	s_waitcnt vmcnt(2)
	v_and_b32_e32 v37, 0xffff0000, v78
	v_and_b32_e32 v39, 0xffff0000, v79
	v_lshlrev_b32_e32 v36, 16, v78
	v_lshlrev_b32_e32 v38, 16, v79
	v_pk_add_f32 v[32:33], v[32:33], v[38:39]
	v_pk_add_f32 v[30:31], v[30:31], v[36:37]
	v_and_b32_e32 v37, 0xffff0000, v80
	v_and_b32_e32 v39, 0xffff0000, v81
	v_lshlrev_b32_e32 v36, 16, v80
	v_lshlrev_b32_e32 v38, 16, v81
	v_pk_add_f32 v[38:39], v[28:29], v[38:39]
	v_pk_add_f32 v[36:37], v[26:27], v[36:37]
	v_cvt_pk_bf16_f32 v26, v30, v31
	v_cvt_pk_bf16_f32 v27, v32, v33
	v_cvt_pk_bf16_f32 v28, v36, v37
	v_cvt_pk_bf16_f32 v29, v38, v39
	global_store_dwordx4 v[100:101], v[26:29], off
	s_waitcnt lgkmcnt(0)
	v_lshlrev_b64 v[34:35], 11, v[98:99]
	v_lshl_add_u64 v[34:35], v[34:35], 0, v[158:159]
	v_mul_f32_e32 v26, v31, v31
	v_mul_f32_e32 v27, v33, v33
	v_fmac_f32_e32 v26, v30, v30
	v_fmac_f32_e32 v27, v32, v32
	v_add_f32_e32 v26, v26, v27
	v_mul_f32_e32 v27, v37, v37
	v_mul_f32_e32 v28, v39, v39
	v_fmac_f32_e32 v27, v36, v36
	v_fmac_f32_e32 v28, v38, v38
	v_add_f32_e32 v27, v27, v28
	v_add_f32_e32 v40, v26, v27
	v_mul_f32_e32 v26, 0x42000000, v30
	v_mul_f32_e32 v27, 0x42000000, v31
	v_med3_f32 v29, v26, s76, v237
	v_med3_f32 v27, v27, s76, v237
	v_mov_b32_e32 v26, v1
	v_cvt_pk_fp8_f32 v26, v29, v27
	v_mul_f32_e32 v28, 0x42000000, v32
	v_mul_f32_e32 v27, 0x42000000, v33
	v_med3_f32 v28, v28, s76, v237
	v_med3_f32 v27, v27, s76, v237
	v_cvt_pk_fp8_f32 v26, v28, v27 op_sel:[0,0,1]
	v_mul_f32_e32 v27, 0x42000000, v36
	v_mul_f32_e32 v28, 0x42000000, v37
	v_med3_f32 v30, v27, s76, v237
	v_med3_f32 v28, v28, s76, v237
	v_mov_b32_e32 v27, v1
	v_cvt_pk_fp8_f32 v27, v30, v28
	v_mul_f32_e32 v29, 0x42000000, v38
	v_mul_f32_e32 v28, 0x42000000, v39
	v_med3_f32 v29, v29, s76, v237
	v_med3_f32 v28, v28, s76, v237
	v_cvt_pk_fp8_f32 v27, v29, v28 op_sel:[0,0,1]
	v_and_b32_e32 v29, 0xffff0000, v74
	v_and_b32_e32 v31, 0xffff0000, v75
	v_lshlrev_b32_e32 v28, 16, v74
	v_lshlrev_b32_e32 v30, 16, v75
	v_pk_add_f32 v[24:25], v[24:25], v[30:31]
	v_pk_add_f32 v[28:29], v[22:23], v[28:29]
	v_and_b32_e32 v23, 0xffff0000, v76
	v_and_b32_e32 v31, 0xffff0000, v77
	v_lshlrev_b32_e32 v22, 16, v76
	v_lshlrev_b32_e32 v30, 16, v77
	v_mul_f32_e32 v32, v29, v29
	v_mul_f32_e32 v33, v25, v25
	v_pk_add_f32 v[30:31], v[20:21], v[30:31]
	v_pk_add_f32 v[18:19], v[18:19], v[22:23]
	v_fmac_f32_e32 v32, v28, v28
	v_fmac_f32_e32 v33, v24, v24
	v_add_f32_e32 v32, v32, v33
	v_mul_f32_e32 v33, v19, v19
	v_mul_f32_e32 v36, v31, v31
	v_fmac_f32_e32 v33, v18, v18
	v_fmac_f32_e32 v36, v30, v30
	v_cvt_pk_bf16_f32 v20, v28, v29
	v_add_f32_e32 v33, v33, v36
	v_mul_f32_e32 v28, 0x42000000, v28
	v_mul_f32_e32 v29, 0x42000000, v29
	v_cvt_pk_bf16_f32 v21, v24, v25
	v_add_f32_e32 v32, v32, v33
	v_mul_f32_e32 v33, 0x42000000, v24
	v_med3_f32 v28, v28, s76, v237
	v_med3_f32 v29, v29, s76, v237
	v_mov_b32_e32 v24, v1
	v_cvt_pk_fp8_f32 v24, v28, v29
	v_mul_f32_e32 v25, 0x42000000, v25
	v_cvt_pk_bf16_f32 v22, v18, v19
	v_med3_f32 v28, v33, s76, v237
	v_med3_f32 v25, v25, s76, v237
	v_mul_f32_e32 v18, 0x42000000, v18
	v_mul_f32_e32 v19, 0x42000000, v19
	v_add_f32_e32 v32, v40, v32
	v_cvt_pk_fp8_f32 v24, v28, v25 op_sel:[0,0,1]
	v_med3_f32 v18, v18, s76, v237
	v_med3_f32 v19, v19, s76, v237
	v_mov_b32_e32 v25, v1
	v_cvt_pk_fp8_f32 v25, v18, v19
	ds_bpermute_b32 v18, v249, v32
	v_mul_f32_e32 v28, 0x42000000, v30
	v_mul_f32_e32 v19, 0x42000000, v31
	v_med3_f32 v28, v28, s76, v237
	v_med3_f32 v19, v19, s76, v237
	s_waitcnt lgkmcnt(0)
	v_add_f32_e32 v18, v32, v18
	v_cvt_pk_fp8_f32 v25, v28, v19 op_sel:[0,0,1]
	ds_bpermute_b32 v19, v250, v18
	v_cvt_pk_bf16_f32 v23, v30, v31
	global_store_dwordx4 v[100:101], v[20:23], off offset:256
	s_nop 1
	v_lshl_add_u64 v[20:21], s[10:11], 0, v[34:35]
	global_store_dwordx2 v[20:21], v[26:27], off
	global_store_dwordx2 v[20:21], v[24:25], off offset:128
	s_and_saveexec_b64 s[24:25], vcc
	s_cbranch_execz .LBB0_5057
	v_lshlrev_b64 v[20:21], 7, v[98:99]
	v_lshl_add_u64 v[20:21], s[12:13], 0, v[20:21]
	v_lshl_add_u64 v[20:21], s[22:23], 2, v[20:21]
	s_lshl_b32 s92, s44, 2
	v_lshl_add_u64 v[20:21], v[20:21], 0, s[92:93]
	s_waitcnt lgkmcnt(0)
	v_add_f32_e32 v18, v18, v19
	global_store_dword v[20:21], v18, off
.LBB0_5057:
	s_or_b64 exec, exec, s[24:25]
	s_waitcnt vmcnt(0)
	v_and_b32_e32 v21, 0xffff0000, v70
	v_and_b32_e32 v23, 0xffff0000, v71
	v_lshlrev_b32_e32 v20, 16, v70
	v_lshlrev_b32_e32 v22, 16, v71
	v_pk_add_f32 v[16:17], v[16:17], v[22:23]
	v_pk_add_f32 v[14:15], v[14:15], v[20:21]
	v_and_b32_e32 v21, 0xffff0000, v72
	v_and_b32_e32 v23, 0xffff0000, v73
	v_lshlrev_b32_e32 v20, 16, v72
	v_lshlrev_b32_e32 v22, 16, v73
	v_pk_add_f32 v[22:23], v[12:13], v[22:23]
	v_pk_add_f32 v[20:21], v[10:11], v[20:21]
	v_cvt_pk_bf16_f32 v10, v14, v15
	v_cvt_pk_bf16_f32 v11, v16, v17
	v_cvt_pk_bf16_f32 v12, v20, v21
	v_cvt_pk_bf16_f32 v13, v22, v23
	global_store_dwordx4 v[96:97], v[10:13], off
	s_waitcnt lgkmcnt(0)
	v_lshlrev_b64 v[18:19], 11, v[94:95]
	v_lshl_add_u64 v[18:19], v[18:19], 0, v[158:159]
	v_mul_f32_e32 v10, v15, v15
	v_mul_f32_e32 v11, v17, v17
	v_fmac_f32_e32 v10, v14, v14
	v_fmac_f32_e32 v11, v16, v16
	v_add_f32_e32 v10, v10, v11
	v_mul_f32_e32 v11, v21, v21
	v_mul_f32_e32 v12, v23, v23
	v_fmac_f32_e32 v11, v20, v20
	v_fmac_f32_e32 v12, v22, v22
	v_add_f32_e32 v11, v11, v12
	v_add_f32_e32 v24, v10, v11
	v_mul_f32_e32 v10, 0x42000000, v14
	v_mul_f32_e32 v11, 0x42000000, v15
	v_med3_f32 v13, v10, s76, v237
	v_med3_f32 v11, v11, s76, v237
	v_mov_b32_e32 v10, v1
	v_cvt_pk_fp8_f32 v10, v13, v11
	v_mul_f32_e32 v12, 0x42000000, v16
	v_mul_f32_e32 v11, 0x42000000, v17
	v_med3_f32 v12, v12, s76, v237
	v_med3_f32 v11, v11, s76, v237
	v_cvt_pk_fp8_f32 v10, v12, v11 op_sel:[0,0,1]
	v_mul_f32_e32 v11, 0x42000000, v20
	v_mul_f32_e32 v12, 0x42000000, v21
	v_med3_f32 v14, v11, s76, v237
	v_med3_f32 v12, v12, s76, v237
	v_mov_b32_e32 v11, v1
	v_cvt_pk_fp8_f32 v11, v14, v12
	v_mul_f32_e32 v13, 0x42000000, v22
	v_mul_f32_e32 v12, 0x42000000, v23
	v_med3_f32 v13, v13, s76, v237
	v_med3_f32 v12, v12, s76, v237
	v_cvt_pk_fp8_f32 v11, v13, v12 op_sel:[0,0,1]
	v_and_b32_e32 v13, 0xffff0000, v66
	v_and_b32_e32 v15, 0xffff0000, v67
	v_lshlrev_b32_e32 v12, 16, v66
	v_lshlrev_b32_e32 v14, 16, v67
	v_pk_add_f32 v[8:9], v[8:9], v[14:15]
	v_pk_add_f32 v[12:13], v[6:7], v[12:13]
	v_and_b32_e32 v7, 0xffff0000, v68
	v_and_b32_e32 v15, 0xffff0000, v69
	v_lshlrev_b32_e32 v6, 16, v68
	v_lshlrev_b32_e32 v14, 16, v69
	v_mul_f32_e32 v16, v13, v13
	v_mul_f32_e32 v17, v9, v9
	v_pk_add_f32 v[14:15], v[4:5], v[14:15]
	v_pk_add_f32 v[2:3], v[2:3], v[6:7]
	v_fmac_f32_e32 v16, v12, v12
	v_fmac_f32_e32 v17, v8, v8
	v_add_f32_e32 v16, v16, v17
	v_mul_f32_e32 v17, v3, v3
	v_mul_f32_e32 v20, v15, v15
	v_fmac_f32_e32 v17, v2, v2
	v_fmac_f32_e32 v20, v14, v14
	v_cvt_pk_bf16_f32 v4, v12, v13
	v_add_f32_e32 v17, v17, v20
	v_mul_f32_e32 v12, 0x42000000, v12
	v_mul_f32_e32 v13, 0x42000000, v13
	v_cvt_pk_bf16_f32 v5, v8, v9
	v_add_f32_e32 v16, v16, v17
	v_mul_f32_e32 v17, 0x42000000, v8
	v_med3_f32 v12, v12, s76, v237
	v_med3_f32 v13, v13, s76, v237
	v_mov_b32_e32 v8, v1
	v_cvt_pk_fp8_f32 v8, v12, v13
	v_mul_f32_e32 v9, 0x42000000, v9
	v_cvt_pk_bf16_f32 v6, v2, v3
	v_med3_f32 v12, v17, s76, v237
	v_med3_f32 v9, v9, s76, v237
	v_mul_f32_e32 v2, 0x42000000, v2
	v_mul_f32_e32 v3, 0x42000000, v3
	v_add_f32_e32 v16, v24, v16
	v_cvt_pk_fp8_f32 v8, v12, v9 op_sel:[0,0,1]
	v_med3_f32 v2, v2, s76, v237
	v_med3_f32 v3, v3, s76, v237
	v_mov_b32_e32 v9, v1
	v_cvt_pk_fp8_f32 v9, v2, v3
	ds_bpermute_b32 v2, v249, v16
	v_mul_f32_e32 v12, 0x42000000, v14
	v_mul_f32_e32 v3, 0x42000000, v15
	v_med3_f32 v12, v12, s76, v237
	v_med3_f32 v3, v3, s76, v237
	s_waitcnt lgkmcnt(0)
	v_add_f32_e32 v2, v16, v2
	v_cvt_pk_fp8_f32 v9, v12, v3 op_sel:[0,0,1]
	ds_bpermute_b32 v3, v250, v2
	v_cvt_pk_bf16_f32 v7, v14, v15
	global_store_dwordx4 v[96:97], v[4:7], off offset:256
	s_nop 1
	v_lshl_add_u64 v[4:5], s[10:11], 0, v[18:19]
	global_store_dwordx2 v[4:5], v[10:11], off
	global_store_dwordx2 v[4:5], v[8:9], off offset:128
	s_and_saveexec_b64 s[24:25], vcc
	s_cbranch_execz .LBB0_5059
	v_lshlrev_b64 v[4:5], 7, v[94:95]
	v_lshl_add_u64 v[4:5], s[12:13], 0, v[4:5]
	v_lshl_add_u64 v[4:5], s[22:23], 2, v[4:5]
	s_lshl_b32 s92, s44, 2
	v_lshl_add_u64 v[4:5], v[4:5], 0, s[92:93]
	s_waitcnt lgkmcnt(0)
	v_add_f32_e32 v2, v2, v3
	global_store_dword v[4:5], v2, off
